# plus pro1 batched loads, expert-count prefix via one load and scalar scan
# speedup vs baseline: 1.0477x; 1.0010x over previous
.LBB0_86:
	global_load_dwordx4 v[18:21], v13, s[10:11]
	global_load_dwordx4 v[128:131], v13, s[10:11] offset:1024
	global_load_dwordx4 v[132:135], v13, s[10:11] offset:2048
	global_load_dwordx4 v[136:139], v13, s[10:11] offset:3072
	s_lshl_b64 s[12:13], s[12:13], 11
	v_lshl_add_u64 v[34:35], v[2:3], 0, s[12:13]
	s_ashr_i32 s2, s0, 31
	s_lshr_b32 s2, s2, 20
	s_add_i32 s2, s0, s2
	s_ashr_i32 s2, s2, 12
	s_and_b64 s[8:9], exec, s[8:9]
	s_cselect_b32 s2, s2, 4
	s_mul_hi_i32 s9, s2, 0x6000
	s_mulk_i32 s2, 0x6000
	s_add_u32 s8, s14, s2
	s_addc_u32 s9, s15, s9
	s_waitcnt vmcnt(3)
	v_cvt_pk_bf16_f32 v22, v18, v19
	v_cvt_pk_bf16_f32 v23, v20, v21
	global_store_dwordx2 v[34:35], v[22:23], off
	s_waitcnt vmcnt(3)
	v_mov_b64_e32 v[22:23], v[128:129]
	v_mov_b64_e32 v[24:25], v[130:131]
	v_pk_mul_f32 v[46:47], v[20:21], v[20:21]
	v_pk_mul_f32 v[48:49], v[18:19], v[18:19]
	s_nop 0
	v_cvt_pk_bf16_f32 v26, v22, v23
	v_cvt_pk_bf16_f32 v27, v24, v25
	global_store_dwordx2 v[34:35], v[26:27], off offset:512
	s_waitcnt vmcnt(3)
	v_mov_b64_e32 v[26:27], v[132:133]
	v_mov_b64_e32 v[28:29], v[134:135]
	v_pk_mov_b32 v[50:51], v[48:49], v[46:47] op_sel:[1,0]
	v_mov_b32_e32 v49, v47
	v_pk_add_f32 v[46:47], v[50:51], v[48:49]
	v_pk_mul_f32 v[48:49], v[24:25], v[24:25]
	v_pk_mul_f32 v[50:51], v[22:23], v[22:23]
	v_pk_add_f32 v[46:47], v[46:47], v[46:47] op_sel:[0,1] op_sel_hi:[1,0]
	v_pk_mov_b32 v[52:53], v[50:51], v[48:49] op_sel:[1,0]
	v_mov_b32_e32 v51, v49
	v_pk_add_f32 v[48:49], v[52:53], v[50:51]
	s_nop 0
	v_cvt_pk_bf16_f32 v30, v26, v27
	v_cvt_pk_bf16_f32 v31, v28, v29
	global_store_dwordx2 v[34:35], v[30:31], off offset:1024
	s_waitcnt vmcnt(3)
	v_mov_b64_e32 v[30:31], v[136:137]
	v_mov_b64_e32 v[32:33], v[138:139]
	s_add_u32 s10, s8, 0x1000
	s_addc_u32 s11, s9, 0
	v_mul_f32_e32 v50, v27, v27
	v_mul_f32_e32 v52, v29, v29
	v_pk_add_f32 v[48:49], v[48:49], v[48:49] op_sel:[0,1] op_sel_hi:[1,0]
	v_pk_fma_f32 v[50:51], v[26:27], v[26:27], v[50:51] op_sel_hi:[1,1,0]
	v_pk_fma_f32 v[52:53], v[28:29], v[28:29], v[52:53] op_sel_hi:[1,1,0]
	s_add_u32 s0, s0, s28
	s_addc_u32 s1, s1, s29
	s_add_u32 s4, s4, s6
	s_addc_u32 s5, s5, s7
	s_cmpk_lt_i32 s0, 0x4400
	s_nop 0
	v_cvt_pk_bf16_f32 v36, v30, v31
	v_cvt_pk_bf16_f32 v37, v32, v33
	global_store_dwordx2 v[34:35], v[36:37], off offset:1536
	global_load_dwordx4 v[34:37], v[4:5], off
	s_nop 0
	global_load_dwordx4 v[38:41], v13, s[10:11]
	global_load_dwordx4 v[42:45], v13, s[8:9]
	global_load_dwordx4 v[140:143], v[4:5], off offset:1024
	global_load_dwordx4 v[144:147], v15, s[10:11]
	global_load_dwordx4 v[148:151], v13, s[8:9] offset:1024
	global_load_dwordx4 v[152:155], v[4:5], off offset:2048
	global_load_dwordx4 v[156:159], v16, s[10:11]
	global_load_dwordx4 v[160:163], v13, s[8:9] offset:2048
	global_load_dwordx4 v[176:179], v[4:5], off offset:3072
	global_load_dwordx4 v[180:183], v17, s[10:11]
	global_load_dwordx4 v[184:187], v13, s[8:9] offset:3072
	v_mul_f32_e32 v47, v30, v30
	v_mul_f32_e32 v49, v31, v31
	v_mul_f32_e32 v51, v32, v32
	v_mul_f32_e32 v53, v33, v33
	v_pk_add_f32 v[46:47], v[46:47], v[48:49]
	v_pk_add_f32 v[48:49], v[50:51], v[52:53]
	s_nop 0
	v_pk_add_f32 v[46:47], v[46:47], v[48:49]
	v_lshl_add_u64 v[48:49], v[6:7], 0, s[12:13]
	v_add_f32_e32 v46, v46, v47
	s_nop 1
	v_mov_b32_dpp v47, v46 quad_perm:[1,0,3,2] row_mask:0xf bank_mask:0xf
	s_waitcnt lgkmcnt(0)
	v_add_f32_e32 v46, v46, v47
	s_nop 1
	v_mov_b32_dpp v47, v46 quad_perm:[2,3,0,1] row_mask:0xf bank_mask:0xf
	s_waitcnt lgkmcnt(0)
	v_add_f32_e32 v46, v46, v47
	s_nop 1
	v_mov_b32_dpp v47, v46 row_half_mirror row_mask:0xf bank_mask:0xf
	s_waitcnt lgkmcnt(0)
	v_add_f32_e32 v46, v46, v47
	s_nop 1
	v_mov_b32_dpp v47, v46 row_mirror row_mask:0xf bank_mask:0xf
	s_waitcnt lgkmcnt(0)
	v_add_f32_e32 v46, v46, v47
	v_mov_b32_e32 v47, v46
	s_nop 1
	v_permlane16_swap_b32_e32 v47, v46
	s_waitcnt lgkmcnt(0)
	v_add_f32_e32 v46, v46, v47
	ds_bpermute_b32 v47, v12, v46
	s_waitcnt lgkmcnt(0)
	v_add_f32_e32 v46, v46, v47
	v_fmamk_f32 v46, v46, 0x3a800000, v14
	v_rsq_f32_e32 v46, v46
	s_nop 0
	v_pk_mul_f32 v[20:21], v[20:21], v[46:47] op_sel_hi:[1,0]
	v_pk_mul_f32 v[18:19], v[18:19], v[46:47] op_sel_hi:[1,0]
	v_pk_mul_f32 v[24:25], v[24:25], v[46:47] op_sel_hi:[1,0]
	v_pk_mul_f32 v[22:23], v[22:23], v[46:47] op_sel_hi:[1,0]
	v_pk_mul_f32 v[28:29], v[28:29], v[46:47] op_sel_hi:[1,0]
	v_pk_mul_f32 v[26:27], v[26:27], v[46:47] op_sel_hi:[1,0]
	v_pk_mul_f32 v[32:33], v[32:33], v[46:47] op_sel_hi:[1,0]
	v_pk_mul_f32 v[30:31], v[30:31], v[46:47] op_sel_hi:[1,0]
	s_waitcnt vmcnt(11)
	v_pk_mul_f32 v[18:19], v[34:35], v[18:19]
	v_pk_mul_f32 v[20:21], v[36:37], v[20:21]
	s_waitcnt vmcnt(10)
	v_pk_add_f32 v[34:35], v[40:41], 1.0 op_sel_hi:[1,0]
	v_pk_add_f32 v[36:37], v[38:39], 1.0 op_sel_hi:[1,0]
	s_waitcnt vmcnt(9)
	v_pk_fma_f32 v[20:21], v[34:35], v[20:21], v[44:45]
	v_pk_fma_f32 v[18:19], v[36:37], v[18:19], v[42:43]
	s_nop 0
	v_cvt_pk_bf16_f32 v18, v18, v19
	v_cvt_pk_bf16_f32 v19, v20, v21
	global_store_dwordx2 v[48:49], v[18:19], off
	s_waitcnt vmcnt(7)
	v_mov_b64_e32 v[18:19], v[140:141]
	v_mov_b64_e32 v[20:21], v[142:143]
	v_mov_b64_e32 v[34:35], v[144:145]
	v_mov_b64_e32 v[36:37], v[146:147]
	v_mov_b64_e32 v[38:39], v[148:149]
	v_mov_b64_e32 v[40:41], v[150:151]
	s_nop 0
	s_nop 0
	s_nop 0
	s_nop 0
	v_pk_mul_f32 v[18:19], v[18:19], v[22:23]
	v_pk_mul_f32 v[20:21], v[20:21], v[24:25]
	s_nop 0
	v_pk_add_f32 v[22:23], v[36:37], 1.0 op_sel_hi:[1,0]
	v_pk_add_f32 v[24:25], v[34:35], 1.0 op_sel_hi:[1,0]
	s_nop 0
	v_pk_fma_f32 v[20:21], v[22:23], v[20:21], v[40:41]
	v_pk_fma_f32 v[18:19], v[24:25], v[18:19], v[38:39]
	s_nop 0
	v_cvt_pk_bf16_f32 v18, v18, v19
	v_cvt_pk_bf16_f32 v19, v20, v21
	global_store_dwordx2 v[48:49], v[18:19], off offset:512
	s_waitcnt vmcnt(5)
	v_mov_b64_e32 v[18:19], v[152:153]
	v_mov_b64_e32 v[20:21], v[154:155]
	v_mov_b64_e32 v[22:23], v[156:157]
	v_mov_b64_e32 v[24:25], v[158:159]
	v_mov_b64_e32 v[34:35], v[160:161]
	v_mov_b64_e32 v[36:37], v[162:163]
	s_nop 0
	s_nop 0
	s_nop 0
	s_nop 0
	v_pk_mul_f32 v[18:19], v[18:19], v[26:27]
	v_pk_mul_f32 v[20:21], v[20:21], v[28:29]
	s_nop 0
	v_pk_add_f32 v[24:25], v[24:25], 1.0 op_sel_hi:[1,0]
	v_pk_add_f32 v[22:23], v[22:23], 1.0 op_sel_hi:[1,0]
	s_nop 0
	v_pk_fma_f32 v[20:21], v[20:21], v[24:25], v[36:37]
	v_pk_fma_f32 v[18:19], v[18:19], v[22:23], v[34:35]
	s_nop 0
	v_cvt_pk_bf16_f32 v18, v18, v19
	v_cvt_pk_bf16_f32 v19, v20, v21
	global_store_dwordx2 v[48:49], v[18:19], off offset:1024
	s_waitcnt vmcnt(3)
	v_mov_b64_e32 v[18:19], v[176:177]
	v_mov_b64_e32 v[20:21], v[178:179]
	v_mov_b64_e32 v[22:23], v[180:181]
	v_mov_b64_e32 v[24:25], v[182:183]
	v_mov_b64_e32 v[26:27], v[184:185]
	v_mov_b64_e32 v[28:29], v[186:187]
	s_nop 0
	s_nop 0
	s_nop 0
	s_nop 0
	v_pk_mul_f32 v[18:19], v[30:31], v[18:19]
	v_pk_mul_f32 v[20:21], v[32:33], v[20:21]
	s_nop 0
	v_pk_add_f32 v[24:25], v[24:25], 1.0 op_sel_hi:[1,0]
	v_pk_add_f32 v[22:23], v[22:23], 1.0 op_sel_hi:[1,0]
	s_nop 0
	v_pk_fma_f32 v[20:21], v[20:21], v[24:25], v[28:29]
	v_pk_fma_f32 v[18:19], v[18:19], v[22:23], v[26:27]
	s_nop 0
	v_cvt_pk_bf16_f32 v18, v18, v19
	v_cvt_pk_bf16_f32 v19, v20, v21
	global_store_dwordx2 v[48:49], v[18:19], off offset:1536
	s_cbranch_scc0 .LBB0_89

.LBB0_1475:
	s_andn2_b64 vcc, exec, s[0:1]
	s_cbranch_vccnz .LBB0_1559
	v_readlane_b32 s0, v255, 37
	v_readlane_b32 s1, v255, 38
	v_mov_b32_e32 v2, v0
	s_lshl_b32 s6, s0, 6
	s_mov_b32 s0, 0
	s_mov_b32 s1, 1
	s_mov_b32 s7, s0
	v_cmp_gt_i32_e64 s[2:3], 32, v2
	v_lshl_add_u32 v6, v2, 2, 0
	s_and_saveexec_b64 s[4:5], s[2:3]
	s_mov_b64 s[18:19], 0x800
	s_cbranch_execz .LBB0_1488
	v_add_u32_e32 v4, 0x20a40, v6
	v_mov_b32_e32 v1, 0
	v_cmp_lt_i32_e32 vcc, 0, v2
	v_add_u32_e32 v3, 0x20c40, v6
	ds_write_b32 v4, v1
	ds_write_b32 v3, v1
	s_mov_b64 s[8:9], exec
	v_readlane_b32 s10, v255, 25
	v_readlane_b32 s11, v255, 26
	s_add_u32 s10, s16, s10
	s_addc_u32 s11, s17, s11
	global_load_dword v8, v6, s[10:11]
	s_mov_b32 s14, 0
	s_waitcnt vmcnt(0)
	v_add_u32_e32 v8, 0xff, v8
	v_and_b32_e32 v8, 0xffffff00, v8
	s_nop 1
	v_readlane_b32 s15, v8, 0
	s_add_u32 s14, s14, s15
	v_writelane_b32 v1, s14, 1
	v_readlane_b32 s15, v8, 1
	s_add_u32 s14, s14, s15
	v_writelane_b32 v1, s14, 2
	v_readlane_b32 s15, v8, 2
	s_add_u32 s14, s14, s15
	v_writelane_b32 v1, s14, 3
	v_readlane_b32 s15, v8, 3
	s_add_u32 s14, s14, s15
	v_writelane_b32 v1, s14, 4
	v_readlane_b32 s15, v8, 4
	s_add_u32 s14, s14, s15
	v_writelane_b32 v1, s14, 5
	v_readlane_b32 s15, v8, 5
	s_add_u32 s14, s14, s15
	v_writelane_b32 v1, s14, 6
	v_readlane_b32 s15, v8, 6
	s_add_u32 s14, s14, s15
	v_writelane_b32 v1, s14, 7
	v_readlane_b32 s15, v8, 7
	s_add_u32 s14, s14, s15
	v_writelane_b32 v1, s14, 8
	v_readlane_b32 s15, v8, 8
	s_add_u32 s14, s14, s15
	v_writelane_b32 v1, s14, 9
	v_readlane_b32 s15, v8, 9
	s_add_u32 s14, s14, s15
	v_writelane_b32 v1, s14, 10
	v_readlane_b32 s15, v8, 10
	s_add_u32 s14, s14, s15
	v_writelane_b32 v1, s14, 11
	v_readlane_b32 s15, v8, 11
	s_add_u32 s14, s14, s15
	v_writelane_b32 v1, s14, 12
	v_readlane_b32 s15, v8, 12
	s_add_u32 s14, s14, s15
	v_writelane_b32 v1, s14, 13
	v_readlane_b32 s15, v8, 13
	s_add_u32 s14, s14, s15
	v_writelane_b32 v1, s14, 14
	v_readlane_b32 s15, v8, 14
	s_add_u32 s14, s14, s15
	v_writelane_b32 v1, s14, 15
	v_readlane_b32 s15, v8, 15
	s_add_u32 s14, s14, s15
	v_writelane_b32 v1, s14, 16
	v_readlane_b32 s15, v8, 16
	s_add_u32 s14, s14, s15
	v_writelane_b32 v1, s14, 17
	v_readlane_b32 s15, v8, 17
	s_add_u32 s14, s14, s15
	v_writelane_b32 v1, s14, 18
	v_readlane_b32 s15, v8, 18
	s_add_u32 s14, s14, s15
	v_writelane_b32 v1, s14, 19
	v_readlane_b32 s15, v8, 19
	s_add_u32 s14, s14, s15
	v_writelane_b32 v1, s14, 20
	v_readlane_b32 s15, v8, 20
	s_add_u32 s14, s14, s15
	v_writelane_b32 v1, s14, 21
	v_readlane_b32 s15, v8, 21
	s_add_u32 s14, s14, s15
	v_writelane_b32 v1, s14, 22
	v_readlane_b32 s15, v8, 22
	s_add_u32 s14, s14, s15
	v_writelane_b32 v1, s14, 23
	v_readlane_b32 s15, v8, 23
	s_add_u32 s14, s14, s15
	v_writelane_b32 v1, s14, 24
	v_readlane_b32 s15, v8, 24
	s_add_u32 s14, s14, s15
	v_writelane_b32 v1, s14, 25
	v_readlane_b32 s15, v8, 25
	s_add_u32 s14, s14, s15
	v_writelane_b32 v1, s14, 26
	v_readlane_b32 s15, v8, 26
	s_add_u32 s14, s14, s15
	v_writelane_b32 v1, s14, 27
	v_readlane_b32 s15, v8, 27
	s_add_u32 s14, s14, s15
	v_writelane_b32 v1, s14, 28
	v_readlane_b32 s15, v8, 28
	s_add_u32 s14, s14, s15
	v_writelane_b32 v1, s14, 29
	v_readlane_b32 s15, v8, 29
	s_add_u32 s14, s14, s15
	v_writelane_b32 v1, s14, 30
	v_readlane_b32 s15, v8, 30
	s_add_u32 s14, s14, s15
	v_writelane_b32 v1, s14, 31

.LBB0_1561:
	s_andn2_b64 vcc, exec, s[0:1]
	s_cbranch_vccnz .LBB0_1641
	v_mov_b32_e32 v2, v0
	s_nop 0
	v_cmp_gt_i32_e32 vcc, 32, v2
	s_and_saveexec_b64 s[2:3], vcc
	v_readlane_b32 s10, v255, 16
	v_readlane_b32 s11, v255, 17
	v_readlane_b32 s14, v255, 18
	s_cbranch_execz .LBB0_1574
	v_mov_b32_e32 v1, 0
	s_mov_b64 s[4:5], exec
	v_readlane_b32 s6, v255, 25
	v_readlane_b32 s7, v255, 26
	s_add_u32 s6, s16, s6
	s_addc_u32 s7, s17, s7
	v_lshlrev_b32_e32 v4, 2, v2
	global_load_dword v6, v4, s[6:7]
	s_mov_b32 s8, 0
	s_waitcnt vmcnt(0)
	v_add_u32_e32 v6, 0xff, v6
	v_and_b32_e32 v6, 0xffffff00, v6
	s_nop 1
	v_readlane_b32 s9, v6, 0
	s_add_u32 s8, s8, s9
	v_writelane_b32 v1, s8, 1
	v_readlane_b32 s9, v6, 1
	s_add_u32 s8, s8, s9
	v_writelane_b32 v1, s8, 2
	v_readlane_b32 s9, v6, 2
	s_add_u32 s8, s8, s9
	v_writelane_b32 v1, s8, 3
	v_readlane_b32 s9, v6, 3
	s_add_u32 s8, s8, s9
	v_writelane_b32 v1, s8, 4
	v_readlane_b32 s9, v6, 4
	s_add_u32 s8, s8, s9
	v_writelane_b32 v1, s8, 5
	v_readlane_b32 s9, v6, 5
	s_add_u32 s8, s8, s9
	v_writelane_b32 v1, s8, 6
	v_readlane_b32 s9, v6, 6
	s_add_u32 s8, s8, s9
	v_writelane_b32 v1, s8, 7
	v_readlane_b32 s9, v6, 7
	s_add_u32 s8, s8, s9
	v_writelane_b32 v1, s8, 8
	v_readlane_b32 s9, v6, 8
	s_add_u32 s8, s8, s9
	v_writelane_b32 v1, s8, 9
	v_readlane_b32 s9, v6, 9
	s_add_u32 s8, s8, s9
	v_writelane_b32 v1, s8, 10
	v_readlane_b32 s9, v6, 10
	s_add_u32 s8, s8, s9
	v_writelane_b32 v1, s8, 11
	v_readlane_b32 s9, v6, 11
	s_add_u32 s8, s8, s9
	v_writelane_b32 v1, s8, 12
	v_readlane_b32 s9, v6, 12
	s_add_u32 s8, s8, s9
	v_writelane_b32 v1, s8, 13
	v_readlane_b32 s9, v6, 13
	s_add_u32 s8, s8, s9
	v_writelane_b32 v1, s8, 14
	v_readlane_b32 s9, v6, 14
	s_add_u32 s8, s8, s9
	v_writelane_b32 v1, s8, 15
	v_readlane_b32 s9, v6, 15
	s_add_u32 s8, s8, s9
	v_writelane_b32 v1, s8, 16
	v_readlane_b32 s9, v6, 16
	s_add_u32 s8, s8, s9
	v_writelane_b32 v1, s8, 17
	v_readlane_b32 s9, v6, 17
	s_add_u32 s8, s8, s9
	v_writelane_b32 v1, s8, 18
	v_readlane_b32 s9, v6, 18
	s_add_u32 s8, s8, s9
	v_writelane_b32 v1, s8, 19
	v_readlane_b32 s9, v6, 19
	s_add_u32 s8, s8, s9
	v_writelane_b32 v1, s8, 20
	v_readlane_b32 s9, v6, 20
	s_add_u32 s8, s8, s9
	v_writelane_b32 v1, s8, 21
	v_readlane_b32 s9, v6, 21
	s_add_u32 s8, s8, s9
	v_writelane_b32 v1, s8, 22
	v_readlane_b32 s9, v6, 22
	s_add_u32 s8, s8, s9
	v_writelane_b32 v1, s8, 23
	v_readlane_b32 s9, v6, 23
	s_add_u32 s8, s8, s9
	v_writelane_b32 v1, s8, 24
	v_readlane_b32 s9, v6, 24
	s_add_u32 s8, s8, s9
	v_writelane_b32 v1, s8, 25
	v_readlane_b32 s9, v6, 25
	s_add_u32 s8, s8, s9
	v_writelane_b32 v1, s8, 26
	v_readlane_b32 s9, v6, 26
	s_add_u32 s8, s8, s9
	v_writelane_b32 v1, s8, 27
	v_readlane_b32 s9, v6, 27
	s_add_u32 s8, s8, s9
	v_writelane_b32 v1, s8, 28
	v_readlane_b32 s9, v6, 28
	s_add_u32 s8, s8, s9
	v_writelane_b32 v1, s8, 29
	v_readlane_b32 s9, v6, 29
	s_add_u32 s8, s8, s9
	v_writelane_b32 v1, s8, 30
	v_readlane_b32 s9, v6, 30
	s_add_u32 s8, s8, s9
	v_writelane_b32 v1, s8, 31
